# speedup vs baseline: 1.0040x; 1.0040x over previous
.Lmg_np:
	v_cndmask_b32_e64 v227, v145, v226, s[0:1]
	v_cndmask_b32_e64 v226, v144, v231, s[0:1]
	v_pk_add_f32 v[224:225], v[226:227], v[224:225]
	v_cndmask_b32_e64 v230, v135, 0, s[0:1]
	v_pk_mul_f32 v[228:229], v[224:225], v[138:139] op_sel:[1,0] op_sel_hi:[0,1]
	v_pk_mov_b32 v[226:227], v[224:225], v[224:225] op_sel:[1,0]
	v_pk_fma_f32 v[224:225], v[224:225], v[136:137], v[228:229]
	v_cndmask_b32_e64 v228, v134, 0, s[0:1]
	v_cndmask_b32_e64 v224, v224, v226, s[0:1]
	v_cndmask_b32_e64 v225, v225, v227, s[0:1]
	v_add_f32_e32 v230, v224, v230
	v_add_f32_e32 v228, v225, v228
	v_lshlrev_b32_e32 v232, 2, v150
	s_add_u32 s44, s18, 0x4000000
	s_addc_u32 s45, s19, 0
	s_add_u32 s46, s18, 0x8000000
	s_addc_u32 s47, s19, 0
	s_mov_b32 s48, 0x3dcccccd
	v_mov_b32_e32 v237, v232
	v_mov_b32_e32 v232, v237
	v_mov_b32_e32 v235, v232
	v_mov_b32_e32 v236, v232
	v_fma_f32 v233, -v130, v131, v82
	v_fmac_f32_e32 v152, 0x3dcccccd, v233
	v_fma_f32 v82, s48, v152, v130
	global_store_dword v232, v82, s[18:19] sc0 sc1
	v_add_u32_e32 v232, 0x1000, v232
	global_store_dword v235, v152, s[44:45] sc0 sc1
	v_add_u32_e32 v235, 0x1000, v235
	global_store_dword v236, v82, s[46:47] sc0 sc1
	v_add_u32_e32 v236, 0x1000, v236
	v_fma_f32 v233, -v82, v131, v83
	v_fmac_f32_e32 v152, 0x3dcccccd, v233
	v_fma_f32 v83, s48, v152, v82
	global_store_dword v232, v83, s[18:19] sc0 sc1
	v_add_u32_e32 v232, 0x1000, v232
	global_store_dword v235, v152, s[44:45] sc0 sc1
	v_add_u32_e32 v235, 0x1000, v235
	global_store_dword v236, v83, s[46:47] sc0 sc1
	v_add_u32_e32 v236, 0x1000, v236
	v_fma_f32 v233, -v83, v131, v84
	v_fmac_f32_e32 v152, 0x3dcccccd, v233
	v_fma_f32 v84, s48, v152, v83
	global_store_dword v232, v84, s[18:19] sc0 sc1
	v_add_u32_e32 v232, 0x1000, v232
	global_store_dword v235, v152, s[44:45] sc0 sc1
	v_add_u32_e32 v235, 0x1000, v235
	global_store_dword v236, v84, s[46:47] sc0 sc1
	v_add_u32_e32 v236, 0x1000, v236
	v_fma_f32 v233, -v84, v131, v85
	v_fmac_f32_e32 v152, 0x3dcccccd, v233
	v_fma_f32 v85, s48, v152, v84
	global_store_dword v232, v85, s[18:19] sc0 sc1
	v_add_u32_e32 v232, 0x1000, v232
	global_store_dword v235, v152, s[44:45] sc0 sc1
	v_add_u32_e32 v235, 0x1000, v235
	global_store_dword v236, v85, s[46:47] sc0 sc1
	v_add_u32_e32 v236, 0x1000, v236
	v_fma_f32 v233, -v85, v131, v86
	v_fmac_f32_e32 v152, 0x3dcccccd, v233
	v_fma_f32 v86, s48, v152, v85
	global_store_dword v232, v86, s[18:19] sc0 sc1
	v_add_u32_e32 v232, 0x1000, v232
	global_store_dword v235, v152, s[44:45] sc0 sc1
	v_add_u32_e32 v235, 0x1000, v235
	global_store_dword v236, v86, s[46:47] sc0 sc1
	v_add_u32_e32 v236, 0x1000, v236
	v_fma_f32 v233, -v86, v131, v87
	v_fmac_f32_e32 v152, 0x3dcccccd, v233
	v_fma_f32 v87, s48, v152, v86
	global_store_dword v232, v87, s[18:19] sc0 sc1
	v_add_u32_e32 v232, 0x1000, v232
	global_store_dword v235, v152, s[44:45] sc0 sc1
	v_add_u32_e32 v235, 0x1000, v235
	global_store_dword v236, v87, s[46:47] sc0 sc1
	v_add_u32_e32 v236, 0x1000, v236
	v_fma_f32 v233, -v87, v131, v88
	v_fmac_f32_e32 v152, 0x3dcccccd, v233
	v_fma_f32 v88, s48, v152, v87
	global_store_dword v232, v88, s[18:19] sc0 sc1
	v_add_u32_e32 v232, 0x1000, v232
	global_store_dword v235, v152, s[44:45] sc0 sc1
	v_add_u32_e32 v235, 0x1000, v235
	global_store_dword v236, v88, s[46:47] sc0 sc1
	v_add_u32_e32 v236, 0x1000, v236
	v_fma_f32 v233, -v88, v131, v89
	v_fmac_f32_e32 v152, 0x3dcccccd, v233
	v_fma_f32 v89, s48, v152, v88
	global_store_dword v232, v89, s[18:19] sc0 sc1
	v_add_u32_e32 v232, 0x1000, v232
	global_store_dword v235, v152, s[44:45] sc0 sc1
	v_add_u32_e32 v235, 0x1000, v235
	global_store_dword v236, v89, s[46:47] sc0 sc1
	v_add_u32_e32 v236, 0x1000, v236
	v_fma_f32 v233, -v89, v131, v90
	v_fmac_f32_e32 v152, 0x3dcccccd, v233
	v_fma_f32 v90, s48, v152, v89
	global_store_dword v232, v90, s[18:19] sc0 sc1
	v_add_u32_e32 v232, 0x1000, v232
	global_store_dword v235, v152, s[44:45] sc0 sc1
	v_add_u32_e32 v235, 0x1000, v235
	global_store_dword v236, v90, s[46:47] sc0 sc1
	v_add_u32_e32 v236, 0x1000, v236
	v_fma_f32 v233, -v90, v131, v91
	v_fmac_f32_e32 v152, 0x3dcccccd, v233
	v_fma_f32 v91, s48, v152, v90
	global_store_dword v232, v91, s[18:19] sc0 sc1
	v_add_u32_e32 v232, 0x1000, v232
	global_store_dword v235, v152, s[44:45] sc0 sc1
	v_add_u32_e32 v235, 0x1000, v235
	global_store_dword v236, v91, s[46:47] sc0 sc1
	v_add_u32_e32 v236, 0x1000, v236
	v_fma_f32 v233, -v91, v131, v92
	v_fmac_f32_e32 v152, 0x3dcccccd, v233
	v_fma_f32 v92, s48, v152, v91
	global_store_dword v232, v92, s[18:19] sc0 sc1
	v_add_u32_e32 v232, 0x1000, v232
	global_store_dword v235, v152, s[44:45] sc0 sc1
	v_add_u32_e32 v235, 0x1000, v235
	global_store_dword v236, v92, s[46:47] sc0 sc1
	v_add_u32_e32 v236, 0x1000, v236
	v_fma_f32 v233, -v92, v131, v93
	v_fmac_f32_e32 v152, 0x3dcccccd, v233
	v_fma_f32 v93, s48, v152, v92
	global_store_dword v232, v93, s[18:19] sc0 sc1
	v_add_u32_e32 v232, 0x1000, v232
	global_store_dword v235, v152, s[44:45] sc0 sc1
	v_add_u32_e32 v235, 0x1000, v235
	global_store_dword v236, v93, s[46:47] sc0 sc1
	v_add_u32_e32 v236, 0x1000, v236
	v_fma_f32 v233, -v93, v131, v94
	v_fmac_f32_e32 v152, 0x3dcccccd, v233
	v_fma_f32 v94, s48, v152, v93
	global_store_dword v232, v94, s[18:19] sc0 sc1
	v_add_u32_e32 v232, 0x1000, v232
	global_store_dword v235, v152, s[44:45] sc0 sc1
	v_add_u32_e32 v235, 0x1000, v235
	global_store_dword v236, v94, s[46:47] sc0 sc1
	v_add_u32_e32 v236, 0x1000, v236
	v_fma_f32 v233, -v94, v131, v95
	v_fmac_f32_e32 v152, 0x3dcccccd, v233
	v_fma_f32 v95, s48, v152, v94
	global_store_dword v232, v95, s[18:19] sc0 sc1
	v_add_u32_e32 v232, 0x1000, v232
	global_store_dword v235, v152, s[44:45] sc0 sc1
	v_add_u32_e32 v235, 0x1000, v235
	global_store_dword v236, v95, s[46:47] sc0 sc1
	v_add_u32_e32 v236, 0x1000, v236
	v_fma_f32 v233, -v95, v131, v96
	v_fmac_f32_e32 v152, 0x3dcccccd, v233
	v_fma_f32 v96, s48, v152, v95
	global_store_dword v232, v96, s[18:19] sc0 sc1
	v_add_u32_e32 v232, 0x1000, v232
	global_store_dword v235, v152, s[44:45] sc0 sc1
	v_add_u32_e32 v235, 0x1000, v235
	global_store_dword v236, v96, s[46:47] sc0 sc1
	v_add_u32_e32 v236, 0x1000, v236
	v_fma_f32 v233, -v96, v131, v97
	v_fmac_f32_e32 v152, 0x3dcccccd, v233
	v_fma_f32 v97, s48, v152, v96
	global_store_dword v232, v97, s[18:19] sc0 sc1
	v_add_u32_e32 v232, 0x1000, v232
	global_store_dword v235, v152, s[44:45] sc0 sc1
	v_add_u32_e32 v235, 0x1000, v235
	global_store_dword v236, v97, s[46:47] sc0 sc1
	v_add_u32_e32 v236, 0x1000, v236
	v_fma_f32 v233, -v97, v131, v114
	v_fmac_f32_e32 v152, 0x3dcccccd, v233
	v_fma_f32 v114, s48, v152, v97
	global_store_dword v232, v114, s[18:19] sc0 sc1
	v_add_u32_e32 v232, 0x1000, v232
	global_store_dword v235, v152, s[44:45] sc0 sc1
	v_add_u32_e32 v235, 0x1000, v235
	global_store_dword v236, v114, s[46:47] sc0 sc1
	v_add_u32_e32 v236, 0x1000, v236
	v_fma_f32 v233, -v114, v131, v115
	v_fmac_f32_e32 v152, 0x3dcccccd, v233
	v_fma_f32 v115, s48, v152, v114
	global_store_dword v232, v115, s[18:19] sc0 sc1
	v_add_u32_e32 v232, 0x1000, v232
	global_store_dword v235, v152, s[44:45] sc0 sc1
	v_add_u32_e32 v235, 0x1000, v235
	global_store_dword v236, v115, s[46:47] sc0 sc1
	v_add_u32_e32 v236, 0x1000, v236
	v_fma_f32 v233, -v115, v131, v116
	v_fmac_f32_e32 v152, 0x3dcccccd, v233
	v_fma_f32 v116, s48, v152, v115
	global_store_dword v232, v116, s[18:19] sc0 sc1
	v_add_u32_e32 v232, 0x1000, v232
	global_store_dword v235, v152, s[44:45] sc0 sc1
	v_add_u32_e32 v235, 0x1000, v235
	global_store_dword v236, v116, s[46:47] sc0 sc1
	v_add_u32_e32 v236, 0x1000, v236
	v_fma_f32 v233, -v116, v131, v117
	v_fmac_f32_e32 v152, 0x3dcccccd, v233
	v_fma_f32 v117, s48, v152, v116
	global_store_dword v232, v117, s[18:19] sc0 sc1
	v_add_u32_e32 v232, 0x1000, v232
	global_store_dword v235, v152, s[44:45] sc0 sc1
	v_add_u32_e32 v235, 0x1000, v235
	global_store_dword v236, v117, s[46:47] sc0 sc1
	v_add_u32_e32 v236, 0x1000, v236
	v_fma_f32 v233, -v117, v131, v118
	v_fmac_f32_e32 v152, 0x3dcccccd, v233
	v_fma_f32 v118, s48, v152, v117
	global_store_dword v232, v118, s[18:19] sc0 sc1
	v_add_u32_e32 v232, 0x1000, v232
	global_store_dword v235, v152, s[44:45] sc0 sc1
	v_add_u32_e32 v235, 0x1000, v235
	global_store_dword v236, v118, s[46:47] sc0 sc1
	v_add_u32_e32 v236, 0x1000, v236
	v_fma_f32 v233, -v118, v131, v119
	v_fmac_f32_e32 v152, 0x3dcccccd, v233
	v_fma_f32 v119, s48, v152, v118
	global_store_dword v232, v119, s[18:19] sc0 sc1
	v_add_u32_e32 v232, 0x1000, v232
	global_store_dword v235, v152, s[44:45] sc0 sc1
	v_add_u32_e32 v235, 0x1000, v235
	global_store_dword v236, v119, s[46:47] sc0 sc1
	v_add_u32_e32 v236, 0x1000, v236
	v_fma_f32 v233, -v119, v131, v120
	v_fmac_f32_e32 v152, 0x3dcccccd, v233
	v_fma_f32 v120, s48, v152, v119
	global_store_dword v232, v120, s[18:19] sc0 sc1
	v_add_u32_e32 v232, 0x1000, v232
	global_store_dword v235, v152, s[44:45] sc0 sc1
	v_add_u32_e32 v235, 0x1000, v235
	global_store_dword v236, v120, s[46:47] sc0 sc1
	v_add_u32_e32 v236, 0x1000, v236
	v_fma_f32 v233, -v120, v131, v121
	v_fmac_f32_e32 v152, 0x3dcccccd, v233
	v_fma_f32 v121, s48, v152, v120
	global_store_dword v232, v121, s[18:19] sc0 sc1
	v_add_u32_e32 v232, 0x1000, v232
	global_store_dword v235, v152, s[44:45] sc0 sc1
	v_add_u32_e32 v235, 0x1000, v235
	global_store_dword v236, v121, s[46:47] sc0 sc1
	v_add_u32_e32 v236, 0x1000, v236
	v_fma_f32 v233, -v121, v131, v122
	v_fmac_f32_e32 v152, 0x3dcccccd, v233
	v_fma_f32 v122, s48, v152, v121
	global_store_dword v232, v122, s[18:19] sc0 sc1
	v_add_u32_e32 v232, 0x1000, v232
	global_store_dword v235, v152, s[44:45] sc0 sc1
	v_add_u32_e32 v235, 0x1000, v235
	global_store_dword v236, v122, s[46:47] sc0 sc1
	v_add_u32_e32 v236, 0x1000, v236
	v_fma_f32 v233, -v122, v131, v123
	v_fmac_f32_e32 v152, 0x3dcccccd, v233
	v_fma_f32 v123, s48, v152, v122
	global_store_dword v232, v123, s[18:19] sc0 sc1
	v_add_u32_e32 v232, 0x1000, v232
	global_store_dword v235, v152, s[44:45] sc0 sc1
	v_add_u32_e32 v235, 0x1000, v235
	global_store_dword v236, v123, s[46:47] sc0 sc1
	v_add_u32_e32 v236, 0x1000, v236
	v_fma_f32 v233, -v123, v131, v124
	v_fmac_f32_e32 v152, 0x3dcccccd, v233
	v_fma_f32 v124, s48, v152, v123
	global_store_dword v232, v124, s[18:19] sc0 sc1
	v_add_u32_e32 v232, 0x1000, v232
	global_store_dword v235, v152, s[44:45] sc0 sc1
	v_add_u32_e32 v235, 0x1000, v235
	global_store_dword v236, v124, s[46:47] sc0 sc1
	v_add_u32_e32 v236, 0x1000, v236
	v_fma_f32 v233, -v124, v131, v125
	v_fmac_f32_e32 v152, 0x3dcccccd, v233
	v_fma_f32 v125, s48, v152, v124
	global_store_dword v232, v125, s[18:19] sc0 sc1
	v_add_u32_e32 v232, 0x1000, v232
	global_store_dword v235, v152, s[44:45] sc0 sc1
	v_add_u32_e32 v235, 0x1000, v235
	global_store_dword v236, v125, s[46:47] sc0 sc1
	v_add_u32_e32 v236, 0x1000, v236
	v_fma_f32 v233, -v125, v131, v126
	v_fmac_f32_e32 v152, 0x3dcccccd, v233
	v_fma_f32 v126, s48, v152, v125
	global_store_dword v232, v126, s[18:19] sc0 sc1
	v_add_u32_e32 v232, 0x1000, v232
	global_store_dword v235, v152, s[44:45] sc0 sc1
	v_add_u32_e32 v235, 0x1000, v235
	global_store_dword v236, v126, s[46:47] sc0 sc1
	v_add_u32_e32 v236, 0x1000, v236
	v_fma_f32 v233, -v126, v131, v127
	v_fmac_f32_e32 v152, 0x3dcccccd, v233
	v_fma_f32 v127, s48, v152, v126
	global_store_dword v232, v127, s[18:19] sc0 sc1
	v_add_u32_e32 v232, 0x1000, v232
	global_store_dword v235, v152, s[44:45] sc0 sc1
	v_add_u32_e32 v235, 0x1000, v235
	global_store_dword v236, v127, s[46:47] sc0 sc1
	v_add_u32_e32 v236, 0x1000, v236
	v_fma_f32 v233, -v127, v131, v128
	v_fmac_f32_e32 v152, 0x3dcccccd, v233
	v_fma_f32 v128, s48, v152, v127
	global_store_dword v232, v128, s[18:19] sc0 sc1
	v_add_u32_e32 v232, 0x1000, v232
	global_store_dword v235, v152, s[44:45] sc0 sc1
	v_add_u32_e32 v235, 0x1000, v235
	global_store_dword v236, v128, s[46:47] sc0 sc1
	v_add_u32_e32 v236, 0x1000, v236
	v_fma_f32 v233, -v128, v131, v129
	v_fmac_f32_e32 v152, 0x3dcccccd, v233
	v_fma_f32 v129, s48, v152, v128
	global_store_dword v232, v129, s[18:19] sc0 sc1
	v_add_u32_e32 v232, 0x1000, v232
	global_store_dword v235, v152, s[44:45] sc0 sc1
	v_add_u32_e32 v235, 0x1000, v235
	global_store_dword v236, v129, s[46:47] sc0 sc1
	v_add_u32_e32 v236, 0x1000, v236
	v_fma_f32 v233, -v129, v131, v98
	v_fmac_f32_e32 v152, 0x3dcccccd, v233
	v_fma_f32 v98, s48, v152, v129
	global_store_dword v232, v98, s[18:19] sc0 sc1
	v_add_u32_e32 v232, 0x1000, v232
	global_store_dword v235, v152, s[44:45] sc0 sc1
	v_add_u32_e32 v235, 0x1000, v235
	global_store_dword v236, v98, s[46:47] sc0 sc1
	v_add_u32_e32 v236, 0x1000, v236
	v_fma_f32 v233, -v98, v131, v99
	v_fmac_f32_e32 v152, 0x3dcccccd, v233
	v_fma_f32 v99, s48, v152, v98
	global_store_dword v232, v99, s[18:19] sc0 sc1
	v_add_u32_e32 v232, 0x1000, v232
	global_store_dword v235, v152, s[44:45] sc0 sc1
	v_add_u32_e32 v235, 0x1000, v235
	global_store_dword v236, v99, s[46:47] sc0 sc1
	v_add_u32_e32 v236, 0x1000, v236
	v_fma_f32 v233, -v99, v131, v100
	v_fmac_f32_e32 v152, 0x3dcccccd, v233
	v_fma_f32 v100, s48, v152, v99
	global_store_dword v232, v100, s[18:19] sc0 sc1
	v_add_u32_e32 v232, 0x1000, v232
	global_store_dword v235, v152, s[44:45] sc0 sc1
	v_add_u32_e32 v235, 0x1000, v235
	global_store_dword v236, v100, s[46:47] sc0 sc1
	v_add_u32_e32 v236, 0x1000, v236
	v_fma_f32 v233, -v100, v131, v101
	v_fmac_f32_e32 v152, 0x3dcccccd, v233
	v_fma_f32 v101, s48, v152, v100
	global_store_dword v232, v101, s[18:19] sc0 sc1
	v_add_u32_e32 v232, 0x1000, v232
	global_store_dword v235, v152, s[44:45] sc0 sc1
	v_add_u32_e32 v235, 0x1000, v235
	global_store_dword v236, v101, s[46:47] sc0 sc1
	v_add_u32_e32 v236, 0x1000, v236
	v_fma_f32 v233, -v101, v131, v102
	v_fmac_f32_e32 v152, 0x3dcccccd, v233
	v_fma_f32 v102, s48, v152, v101
	global_store_dword v232, v102, s[18:19] sc0 sc1
	v_add_u32_e32 v232, 0x1000, v232
	global_store_dword v235, v152, s[44:45] sc0 sc1
	v_add_u32_e32 v235, 0x1000, v235
	global_store_dword v236, v102, s[46:47] sc0 sc1
	v_add_u32_e32 v236, 0x1000, v236
	v_fma_f32 v233, -v102, v131, v103
	v_fmac_f32_e32 v152, 0x3dcccccd, v233
	v_fma_f32 v103, s48, v152, v102
	global_store_dword v232, v103, s[18:19] sc0 sc1
	v_add_u32_e32 v232, 0x1000, v232
	global_store_dword v235, v152, s[44:45] sc0 sc1
	v_add_u32_e32 v235, 0x1000, v235
	global_store_dword v236, v103, s[46:47] sc0 sc1
	v_add_u32_e32 v236, 0x1000, v236
	v_fma_f32 v233, -v103, v131, v104
	v_fmac_f32_e32 v152, 0x3dcccccd, v233
	v_fma_f32 v104, s48, v152, v103
	global_store_dword v232, v104, s[18:19] sc0 sc1
	v_add_u32_e32 v232, 0x1000, v232
	global_store_dword v235, v152, s[44:45] sc0 sc1
	v_add_u32_e32 v235, 0x1000, v235
	global_store_dword v236, v104, s[46:47] sc0 sc1
	v_add_u32_e32 v236, 0x1000, v236
	v_fma_f32 v233, -v104, v131, v105
	v_fmac_f32_e32 v152, 0x3dcccccd, v233
	v_fma_f32 v105, s48, v152, v104
	global_store_dword v232, v105, s[18:19] sc0 sc1
	v_add_u32_e32 v232, 0x1000, v232
	global_store_dword v235, v152, s[44:45] sc0 sc1
	v_add_u32_e32 v235, 0x1000, v235
	global_store_dword v236, v105, s[46:47] sc0 sc1
	v_add_u32_e32 v236, 0x1000, v236
	v_fma_f32 v233, -v105, v131, v106
	v_fmac_f32_e32 v152, 0x3dcccccd, v233
	v_fma_f32 v106, s48, v152, v105
	global_store_dword v232, v106, s[18:19] sc0 sc1
	v_add_u32_e32 v232, 0x1000, v232
	global_store_dword v235, v152, s[44:45] sc0 sc1
	v_add_u32_e32 v235, 0x1000, v235
	global_store_dword v236, v106, s[46:47] sc0 sc1
	v_add_u32_e32 v236, 0x1000, v236
	v_fma_f32 v233, -v106, v131, v107
	v_fmac_f32_e32 v152, 0x3dcccccd, v233
	v_fma_f32 v107, s48, v152, v106
	global_store_dword v232, v107, s[18:19] sc0 sc1
	v_add_u32_e32 v232, 0x1000, v232
	global_store_dword v235, v152, s[44:45] sc0 sc1
	v_add_u32_e32 v235, 0x1000, v235
	global_store_dword v236, v107, s[46:47] sc0 sc1
	v_add_u32_e32 v236, 0x1000, v236
	v_fma_f32 v233, -v107, v131, v108
	v_fmac_f32_e32 v152, 0x3dcccccd, v233
	v_fma_f32 v108, s48, v152, v107
	global_store_dword v232, v108, s[18:19] sc0 sc1
	v_add_u32_e32 v232, 0x1000, v232
	global_store_dword v235, v152, s[44:45] sc0 sc1
	v_add_u32_e32 v235, 0x1000, v235
	global_store_dword v236, v108, s[46:47] sc0 sc1
	v_add_u32_e32 v236, 0x1000, v236
	v_fma_f32 v233, -v108, v131, v109
	v_fmac_f32_e32 v152, 0x3dcccccd, v233
	v_fma_f32 v109, s48, v152, v108
	global_store_dword v232, v109, s[18:19] sc0 sc1
	v_add_u32_e32 v232, 0x1000, v232
	global_store_dword v235, v152, s[44:45] sc0 sc1
	v_add_u32_e32 v235, 0x1000, v235
	global_store_dword v236, v109, s[46:47] sc0 sc1
	v_add_u32_e32 v236, 0x1000, v236
	v_fma_f32 v233, -v109, v131, v110
	v_fmac_f32_e32 v152, 0x3dcccccd, v233
	v_fma_f32 v110, s48, v152, v109
	global_store_dword v232, v110, s[18:19] sc0 sc1
	v_add_u32_e32 v232, 0x1000, v232
	global_store_dword v235, v152, s[44:45] sc0 sc1
	v_add_u32_e32 v235, 0x1000, v235
	global_store_dword v236, v110, s[46:47] sc0 sc1
	v_add_u32_e32 v236, 0x1000, v236
	v_fma_f32 v233, -v110, v131, v111
	v_fmac_f32_e32 v152, 0x3dcccccd, v233
	v_fma_f32 v111, s48, v152, v110
	global_store_dword v232, v111, s[18:19] sc0 sc1
	v_add_u32_e32 v232, 0x1000, v232
	global_store_dword v235, v152, s[44:45] sc0 sc1
	v_add_u32_e32 v235, 0x1000, v235
	global_store_dword v236, v111, s[46:47] sc0 sc1
	v_add_u32_e32 v236, 0x1000, v236
	v_fma_f32 v233, -v111, v131, v112
	v_fmac_f32_e32 v152, 0x3dcccccd, v233
	v_fma_f32 v112, s48, v152, v111
	global_store_dword v232, v112, s[18:19] sc0 sc1
	v_add_u32_e32 v232, 0x1000, v232
	global_store_dword v235, v152, s[44:45] sc0 sc1
	v_add_u32_e32 v235, 0x1000, v235
	global_store_dword v236, v112, s[46:47] sc0 sc1
	v_add_u32_e32 v236, 0x1000, v236
	v_fma_f32 v233, -v112, v131, v113
	v_fmac_f32_e32 v152, 0x3dcccccd, v233
	v_fma_f32 v113, s48, v152, v112
	global_store_dword v232, v113, s[18:19] sc0 sc1
	v_add_u32_e32 v232, 0x1000, v232
	global_store_dword v235, v152, s[44:45] sc0 sc1
	v_add_u32_e32 v235, 0x1000, v235
	global_store_dword v236, v113, s[46:47] sc0 sc1
	v_add_u32_e32 v236, 0x1000, v236
	v_fma_f32 v233, -v113, v131, v66
	v_fmac_f32_e32 v152, 0x3dcccccd, v233
	v_fma_f32 v66, s48, v152, v113
	global_store_dword v232, v66, s[18:19] sc0 sc1
	v_add_u32_e32 v232, 0x1000, v232
	global_store_dword v235, v152, s[44:45] sc0 sc1
	v_add_u32_e32 v235, 0x1000, v235
	global_store_dword v236, v66, s[46:47] sc0 sc1
	v_add_u32_e32 v236, 0x1000, v236
	v_fma_f32 v233, -v66, v131, v67
	v_fmac_f32_e32 v152, 0x3dcccccd, v233
	v_fma_f32 v67, s48, v152, v66
	global_store_dword v232, v67, s[18:19] sc0 sc1
	v_add_u32_e32 v232, 0x1000, v232
	global_store_dword v235, v152, s[44:45] sc0 sc1
	v_add_u32_e32 v235, 0x1000, v235
	global_store_dword v236, v67, s[46:47] sc0 sc1
	v_add_u32_e32 v236, 0x1000, v236
	v_fma_f32 v233, -v67, v131, v68
	v_fmac_f32_e32 v152, 0x3dcccccd, v233
	v_fma_f32 v68, s48, v152, v67
	global_store_dword v232, v68, s[18:19] sc0 sc1
	v_add_u32_e32 v232, 0x1000, v232
	global_store_dword v235, v152, s[44:45] sc0 sc1
	v_add_u32_e32 v235, 0x1000, v235
	global_store_dword v236, v68, s[46:47] sc0 sc1
	v_add_u32_e32 v236, 0x1000, v236
	v_fma_f32 v233, -v68, v131, v69
	v_fmac_f32_e32 v152, 0x3dcccccd, v233
	v_fma_f32 v69, s48, v152, v68
	global_store_dword v232, v69, s[18:19] sc0 sc1
	v_add_u32_e32 v232, 0x1000, v232
	global_store_dword v235, v152, s[44:45] sc0 sc1
	v_add_u32_e32 v235, 0x1000, v235
	global_store_dword v236, v69, s[46:47] sc0 sc1
	v_add_u32_e32 v236, 0x1000, v236
	v_fma_f32 v233, -v69, v131, v70
	v_fmac_f32_e32 v152, 0x3dcccccd, v233
	v_fma_f32 v70, s48, v152, v69
	global_store_dword v232, v70, s[18:19] sc0 sc1
	v_add_u32_e32 v232, 0x1000, v232
	global_store_dword v235, v152, s[44:45] sc0 sc1
	v_add_u32_e32 v235, 0x1000, v235
	global_store_dword v236, v70, s[46:47] sc0 sc1
	v_add_u32_e32 v236, 0x1000, v236
	v_fma_f32 v233, -v70, v131, v71
	v_fmac_f32_e32 v152, 0x3dcccccd, v233
	v_fma_f32 v71, s48, v152, v70
	global_store_dword v232, v71, s[18:19] sc0 sc1
	v_add_u32_e32 v232, 0x1000, v232
	global_store_dword v235, v152, s[44:45] sc0 sc1
	v_add_u32_e32 v235, 0x1000, v235
	global_store_dword v236, v71, s[46:47] sc0 sc1
	v_add_u32_e32 v236, 0x1000, v236
	v_fma_f32 v233, -v71, v131, v72
	v_fmac_f32_e32 v152, 0x3dcccccd, v233
	v_fma_f32 v72, s48, v152, v71
	global_store_dword v232, v72, s[18:19] sc0 sc1
	v_add_u32_e32 v232, 0x1000, v232
	global_store_dword v235, v152, s[44:45] sc0 sc1
	v_add_u32_e32 v235, 0x1000, v235
	global_store_dword v236, v72, s[46:47] sc0 sc1
	v_add_u32_e32 v236, 0x1000, v236
	v_fma_f32 v233, -v72, v131, v73
	v_fmac_f32_e32 v152, 0x3dcccccd, v233
	v_fma_f32 v73, s48, v152, v72
	global_store_dword v232, v73, s[18:19] sc0 sc1
	v_add_u32_e32 v232, 0x1000, v232
	global_store_dword v235, v152, s[44:45] sc0 sc1
	v_add_u32_e32 v235, 0x1000, v235
	global_store_dword v236, v73, s[46:47] sc0 sc1
	v_add_u32_e32 v236, 0x1000, v236
	v_fma_f32 v233, -v73, v131, v74
	v_fmac_f32_e32 v152, 0x3dcccccd, v233
	v_fma_f32 v74, s48, v152, v73
	global_store_dword v232, v74, s[18:19] sc0 sc1
	v_add_u32_e32 v232, 0x1000, v232
	global_store_dword v235, v152, s[44:45] sc0 sc1
	v_add_u32_e32 v235, 0x1000, v235
	global_store_dword v236, v74, s[46:47] sc0 sc1
	v_add_u32_e32 v236, 0x1000, v236
	v_fma_f32 v233, -v74, v131, v75
	v_fmac_f32_e32 v152, 0x3dcccccd, v233
	v_fma_f32 v75, s48, v152, v74
	global_store_dword v232, v75, s[18:19] sc0 sc1
	v_add_u32_e32 v232, 0x1000, v232
	global_store_dword v235, v152, s[44:45] sc0 sc1
	v_add_u32_e32 v235, 0x1000, v235
	global_store_dword v236, v75, s[46:47] sc0 sc1
	v_add_u32_e32 v236, 0x1000, v236
	v_fma_f32 v233, -v75, v131, v76
	v_fmac_f32_e32 v152, 0x3dcccccd, v233
	v_fma_f32 v76, s48, v152, v75
	global_store_dword v232, v76, s[18:19] sc0 sc1
	v_add_u32_e32 v232, 0x1000, v232
	global_store_dword v235, v152, s[44:45] sc0 sc1
	v_add_u32_e32 v235, 0x1000, v235
	global_store_dword v236, v76, s[46:47] sc0 sc1
	v_add_u32_e32 v236, 0x1000, v236
	v_fma_f32 v233, -v76, v131, v77
	v_fmac_f32_e32 v152, 0x3dcccccd, v233
	v_fma_f32 v77, s48, v152, v76
	global_store_dword v232, v77, s[18:19] sc0 sc1
	v_add_u32_e32 v232, 0x1000, v232
	global_store_dword v235, v152, s[44:45] sc0 sc1
	v_add_u32_e32 v235, 0x1000, v235
	global_store_dword v236, v77, s[46:47] sc0 sc1
	v_add_u32_e32 v236, 0x1000, v236
	v_fma_f32 v233, -v77, v131, v78
	v_fmac_f32_e32 v152, 0x3dcccccd, v233
	v_fma_f32 v78, s48, v152, v77
	global_store_dword v232, v78, s[18:19] sc0 sc1
	v_add_u32_e32 v232, 0x1000, v232
	global_store_dword v235, v152, s[44:45] sc0 sc1
	v_add_u32_e32 v235, 0x1000, v235
	global_store_dword v236, v78, s[46:47] sc0 sc1
	v_add_u32_e32 v236, 0x1000, v236
	v_fma_f32 v233, -v78, v131, v79
	v_fmac_f32_e32 v152, 0x3dcccccd, v233
	v_fma_f32 v79, s48, v152, v78
	global_store_dword v232, v79, s[18:19] sc0 sc1
	v_add_u32_e32 v232, 0x1000, v232
	global_store_dword v235, v152, s[44:45] sc0 sc1
	v_add_u32_e32 v235, 0x1000, v235
	global_store_dword v236, v79, s[46:47] sc0 sc1
	v_add_u32_e32 v236, 0x1000, v236
	v_fma_f32 v233, -v79, v131, v80
	v_fmac_f32_e32 v152, 0x3dcccccd, v233
	v_fma_f32 v80, s48, v152, v79
	global_store_dword v232, v80, s[18:19] sc0 sc1
	v_add_u32_e32 v232, 0x1000, v232
	global_store_dword v235, v152, s[44:45] sc0 sc1
	v_add_u32_e32 v235, 0x1000, v235
	global_store_dword v236, v80, s[46:47] sc0 sc1
	v_add_u32_e32 v236, 0x1000, v236
	v_fma_f32 v233, -v80, v131, v81
	v_fmac_f32_e32 v152, 0x3dcccccd, v233
	v_fma_f32 v81, s48, v152, v80
	global_store_dword v232, v81, s[18:19] sc0 sc1
	v_add_u32_e32 v232, 0x1000, v232
	global_store_dword v235, v152, s[44:45] sc0 sc1
	v_add_u32_e32 v235, 0x1000, v235
	global_store_dword v236, v81, s[46:47] sc0 sc1
	v_add_u32_e32 v236, 0x1000, v236
	v_add_u32_e32 v232, 0x80, v237
	v_mov_b32_e32 v235, v232
	v_mov_b32_e32 v236, v232
	v_fma_f32 v233, -v230, v1, v50
	v_fmac_f32_e32 v228, 0x3dcccccd, v233
	v_fma_f32 v50, s48, v228, v230
	global_store_dword v232, v50, s[18:19] sc0 sc1
	v_add_u32_e32 v232, 0x1000, v232
	global_store_dword v235, v228, s[44:45] sc0 sc1
	v_add_u32_e32 v235, 0x1000, v235
	global_store_dword v236, v50, s[46:47] sc0 sc1
	v_add_u32_e32 v236, 0x1000, v236
	v_fma_f32 v233, -v50, v1, v51
	v_fmac_f32_e32 v228, 0x3dcccccd, v233
	v_fma_f32 v51, s48, v228, v50
	global_store_dword v232, v51, s[18:19] sc0 sc1
	v_add_u32_e32 v232, 0x1000, v232
	global_store_dword v235, v228, s[44:45] sc0 sc1
	v_add_u32_e32 v235, 0x1000, v235
	global_store_dword v236, v51, s[46:47] sc0 sc1
	v_add_u32_e32 v236, 0x1000, v236
	v_fma_f32 v233, -v51, v1, v52
	v_fmac_f32_e32 v228, 0x3dcccccd, v233
	v_fma_f32 v52, s48, v228, v51
	global_store_dword v232, v52, s[18:19] sc0 sc1
	v_add_u32_e32 v232, 0x1000, v232
	global_store_dword v235, v228, s[44:45] sc0 sc1
	v_add_u32_e32 v235, 0x1000, v235
	global_store_dword v236, v52, s[46:47] sc0 sc1
	v_add_u32_e32 v236, 0x1000, v236
	v_fma_f32 v233, -v52, v1, v53
	v_fmac_f32_e32 v228, 0x3dcccccd, v233
	v_fma_f32 v53, s48, v228, v52
	global_store_dword v232, v53, s[18:19] sc0 sc1
	v_add_u32_e32 v232, 0x1000, v232
	global_store_dword v235, v228, s[44:45] sc0 sc1
	v_add_u32_e32 v235, 0x1000, v235
	global_store_dword v236, v53, s[46:47] sc0 sc1
	v_add_u32_e32 v236, 0x1000, v236
	v_fma_f32 v233, -v53, v1, v54
	v_fmac_f32_e32 v228, 0x3dcccccd, v233
	v_fma_f32 v54, s48, v228, v53
	global_store_dword v232, v54, s[18:19] sc0 sc1
	v_add_u32_e32 v232, 0x1000, v232
	global_store_dword v235, v228, s[44:45] sc0 sc1
	v_add_u32_e32 v235, 0x1000, v235
	global_store_dword v236, v54, s[46:47] sc0 sc1
	v_add_u32_e32 v236, 0x1000, v236
	v_fma_f32 v233, -v54, v1, v55
	v_fmac_f32_e32 v228, 0x3dcccccd, v233
	v_fma_f32 v55, s48, v228, v54
	global_store_dword v232, v55, s[18:19] sc0 sc1
	v_add_u32_e32 v232, 0x1000, v232
	global_store_dword v235, v228, s[44:45] sc0 sc1
	v_add_u32_e32 v235, 0x1000, v235
	global_store_dword v236, v55, s[46:47] sc0 sc1
	v_add_u32_e32 v236, 0x1000, v236
	v_fma_f32 v233, -v55, v1, v56
	v_fmac_f32_e32 v228, 0x3dcccccd, v233
	v_fma_f32 v56, s48, v228, v55
	global_store_dword v232, v56, s[18:19] sc0 sc1
	v_add_u32_e32 v232, 0x1000, v232
	global_store_dword v235, v228, s[44:45] sc0 sc1
	v_add_u32_e32 v235, 0x1000, v235
	global_store_dword v236, v56, s[46:47] sc0 sc1
	v_add_u32_e32 v236, 0x1000, v236
	v_fma_f32 v233, -v56, v1, v57
	v_fmac_f32_e32 v228, 0x3dcccccd, v233
	v_fma_f32 v57, s48, v228, v56
	global_store_dword v232, v57, s[18:19] sc0 sc1
	v_add_u32_e32 v232, 0x1000, v232
	global_store_dword v235, v228, s[44:45] sc0 sc1
	v_add_u32_e32 v235, 0x1000, v235
	global_store_dword v236, v57, s[46:47] sc0 sc1
	v_add_u32_e32 v236, 0x1000, v236
	v_fma_f32 v233, -v57, v1, v58
	v_fmac_f32_e32 v228, 0x3dcccccd, v233
	v_fma_f32 v58, s48, v228, v57
	global_store_dword v232, v58, s[18:19] sc0 sc1
	v_add_u32_e32 v232, 0x1000, v232
	global_store_dword v235, v228, s[44:45] sc0 sc1
	v_add_u32_e32 v235, 0x1000, v235
	global_store_dword v236, v58, s[46:47] sc0 sc1
	v_add_u32_e32 v236, 0x1000, v236
	v_fma_f32 v233, -v58, v1, v59
	v_fmac_f32_e32 v228, 0x3dcccccd, v233
	v_fma_f32 v59, s48, v228, v58
	global_store_dword v232, v59, s[18:19] sc0 sc1
	v_add_u32_e32 v232, 0x1000, v232
	global_store_dword v235, v228, s[44:45] sc0 sc1
	v_add_u32_e32 v235, 0x1000, v235
	global_store_dword v236, v59, s[46:47] sc0 sc1
	v_add_u32_e32 v236, 0x1000, v236
	v_fma_f32 v233, -v59, v1, v60
	v_fmac_f32_e32 v228, 0x3dcccccd, v233
	v_fma_f32 v60, s48, v228, v59
	global_store_dword v232, v60, s[18:19] sc0 sc1
	v_add_u32_e32 v232, 0x1000, v232
	global_store_dword v235, v228, s[44:45] sc0 sc1
	v_add_u32_e32 v235, 0x1000, v235
	global_store_dword v236, v60, s[46:47] sc0 sc1
	v_add_u32_e32 v236, 0x1000, v236
	v_fma_f32 v233, -v60, v1, v61
	v_fmac_f32_e32 v228, 0x3dcccccd, v233
	v_fma_f32 v61, s48, v228, v60
	global_store_dword v232, v61, s[18:19] sc0 sc1
	v_add_u32_e32 v232, 0x1000, v232
	global_store_dword v235, v228, s[44:45] sc0 sc1
	v_add_u32_e32 v235, 0x1000, v235
	global_store_dword v236, v61, s[46:47] sc0 sc1
	v_add_u32_e32 v236, 0x1000, v236
	v_fma_f32 v233, -v61, v1, v62
	v_fmac_f32_e32 v228, 0x3dcccccd, v233
	v_fma_f32 v62, s48, v228, v61
	global_store_dword v232, v62, s[18:19] sc0 sc1
	v_add_u32_e32 v232, 0x1000, v232
	global_store_dword v235, v228, s[44:45] sc0 sc1
	v_add_u32_e32 v235, 0x1000, v235
	global_store_dword v236, v62, s[46:47] sc0 sc1
	v_add_u32_e32 v236, 0x1000, v236
	v_fma_f32 v233, -v62, v1, v63
	v_fmac_f32_e32 v228, 0x3dcccccd, v233
	v_fma_f32 v63, s48, v228, v62
	global_store_dword v232, v63, s[18:19] sc0 sc1
	v_add_u32_e32 v232, 0x1000, v232
	global_store_dword v235, v228, s[44:45] sc0 sc1
	v_add_u32_e32 v235, 0x1000, v235
	global_store_dword v236, v63, s[46:47] sc0 sc1
	v_add_u32_e32 v236, 0x1000, v236
	v_fma_f32 v233, -v63, v1, v64
	v_fmac_f32_e32 v228, 0x3dcccccd, v233
	v_fma_f32 v64, s48, v228, v63
	global_store_dword v232, v64, s[18:19] sc0 sc1
	v_add_u32_e32 v232, 0x1000, v232
	global_store_dword v235, v228, s[44:45] sc0 sc1
	v_add_u32_e32 v235, 0x1000, v235
	global_store_dword v236, v64, s[46:47] sc0 sc1
	v_add_u32_e32 v236, 0x1000, v236
	v_fma_f32 v233, -v64, v1, v65
	v_fmac_f32_e32 v228, 0x3dcccccd, v233
	v_fma_f32 v65, s48, v228, v64
	global_store_dword v232, v65, s[18:19] sc0 sc1
	v_add_u32_e32 v232, 0x1000, v232
	global_store_dword v235, v228, s[44:45] sc0 sc1
	v_add_u32_e32 v235, 0x1000, v235
	global_store_dword v236, v65, s[46:47] sc0 sc1
	v_add_u32_e32 v236, 0x1000, v236
	v_fma_f32 v233, -v65, v1, v34
	v_fmac_f32_e32 v228, 0x3dcccccd, v233
	v_fma_f32 v34, s48, v228, v65
	global_store_dword v232, v34, s[18:19] sc0 sc1
	v_add_u32_e32 v232, 0x1000, v232
	global_store_dword v235, v228, s[44:45] sc0 sc1
	v_add_u32_e32 v235, 0x1000, v235
	global_store_dword v236, v34, s[46:47] sc0 sc1
	v_add_u32_e32 v236, 0x1000, v236
	v_fma_f32 v233, -v34, v1, v35
	v_fmac_f32_e32 v228, 0x3dcccccd, v233
	v_fma_f32 v35, s48, v228, v34
	global_store_dword v232, v35, s[18:19] sc0 sc1
	v_add_u32_e32 v232, 0x1000, v232
	global_store_dword v235, v228, s[44:45] sc0 sc1
	v_add_u32_e32 v235, 0x1000, v235
	global_store_dword v236, v35, s[46:47] sc0 sc1
	v_add_u32_e32 v236, 0x1000, v236
	v_fma_f32 v233, -v35, v1, v36
	v_fmac_f32_e32 v228, 0x3dcccccd, v233
	v_fma_f32 v36, s48, v228, v35
	global_store_dword v232, v36, s[18:19] sc0 sc1
	v_add_u32_e32 v232, 0x1000, v232
	global_store_dword v235, v228, s[44:45] sc0 sc1
	v_add_u32_e32 v235, 0x1000, v235
	global_store_dword v236, v36, s[46:47] sc0 sc1
	v_add_u32_e32 v236, 0x1000, v236
	v_fma_f32 v233, -v36, v1, v37
	v_fmac_f32_e32 v228, 0x3dcccccd, v233
	v_fma_f32 v37, s48, v228, v36
	global_store_dword v232, v37, s[18:19] sc0 sc1
	v_add_u32_e32 v232, 0x1000, v232
	global_store_dword v235, v228, s[44:45] sc0 sc1
	v_add_u32_e32 v235, 0x1000, v235
	global_store_dword v236, v37, s[46:47] sc0 sc1
	v_add_u32_e32 v236, 0x1000, v236
	v_fma_f32 v233, -v37, v1, v38
	v_fmac_f32_e32 v228, 0x3dcccccd, v233
	v_fma_f32 v38, s48, v228, v37
	global_store_dword v232, v38, s[18:19] sc0 sc1
	v_add_u32_e32 v232, 0x1000, v232
	global_store_dword v235, v228, s[44:45] sc0 sc1
	v_add_u32_e32 v235, 0x1000, v235
	global_store_dword v236, v38, s[46:47] sc0 sc1
	v_add_u32_e32 v236, 0x1000, v236
	v_fma_f32 v233, -v38, v1, v39
	v_fmac_f32_e32 v228, 0x3dcccccd, v233
	v_fma_f32 v39, s48, v228, v38
	global_store_dword v232, v39, s[18:19] sc0 sc1
	v_add_u32_e32 v232, 0x1000, v232
	global_store_dword v235, v228, s[44:45] sc0 sc1
	v_add_u32_e32 v235, 0x1000, v235
	global_store_dword v236, v39, s[46:47] sc0 sc1
	v_add_u32_e32 v236, 0x1000, v236
	v_fma_f32 v233, -v39, v1, v40
	v_fmac_f32_e32 v228, 0x3dcccccd, v233
	v_fma_f32 v40, s48, v228, v39
	global_store_dword v232, v40, s[18:19] sc0 sc1
	v_add_u32_e32 v232, 0x1000, v232
	global_store_dword v235, v228, s[44:45] sc0 sc1
	v_add_u32_e32 v235, 0x1000, v235
	global_store_dword v236, v40, s[46:47] sc0 sc1
	v_add_u32_e32 v236, 0x1000, v236
	v_fma_f32 v233, -v40, v1, v41
	v_fmac_f32_e32 v228, 0x3dcccccd, v233
	v_fma_f32 v41, s48, v228, v40
	global_store_dword v232, v41, s[18:19] sc0 sc1
	v_add_u32_e32 v232, 0x1000, v232
	global_store_dword v235, v228, s[44:45] sc0 sc1
	v_add_u32_e32 v235, 0x1000, v235
	global_store_dword v236, v41, s[46:47] sc0 sc1
	v_add_u32_e32 v236, 0x1000, v236
	v_fma_f32 v233, -v41, v1, v42
	v_fmac_f32_e32 v228, 0x3dcccccd, v233
	v_fma_f32 v42, s48, v228, v41
	global_store_dword v232, v42, s[18:19] sc0 sc1
	v_add_u32_e32 v232, 0x1000, v232
	global_store_dword v235, v228, s[44:45] sc0 sc1
	v_add_u32_e32 v235, 0x1000, v235
	global_store_dword v236, v42, s[46:47] sc0 sc1
	v_add_u32_e32 v236, 0x1000, v236
	v_fma_f32 v233, -v42, v1, v43
	v_fmac_f32_e32 v228, 0x3dcccccd, v233
	v_fma_f32 v43, s48, v228, v42
	global_store_dword v232, v43, s[18:19] sc0 sc1
	v_add_u32_e32 v232, 0x1000, v232
	global_store_dword v235, v228, s[44:45] sc0 sc1
	v_add_u32_e32 v235, 0x1000, v235
	global_store_dword v236, v43, s[46:47] sc0 sc1
	v_add_u32_e32 v236, 0x1000, v236
	v_fma_f32 v233, -v43, v1, v44
	v_fmac_f32_e32 v228, 0x3dcccccd, v233
	v_fma_f32 v44, s48, v228, v43
	global_store_dword v232, v44, s[18:19] sc0 sc1
	v_add_u32_e32 v232, 0x1000, v232
	global_store_dword v235, v228, s[44:45] sc0 sc1
	v_add_u32_e32 v235, 0x1000, v235
	global_store_dword v236, v44, s[46:47] sc0 sc1
	v_add_u32_e32 v236, 0x1000, v236
	v_fma_f32 v233, -v44, v1, v45
	v_fmac_f32_e32 v228, 0x3dcccccd, v233
	v_fma_f32 v45, s48, v228, v44
	global_store_dword v232, v45, s[18:19] sc0 sc1
	v_add_u32_e32 v232, 0x1000, v232
	global_store_dword v235, v228, s[44:45] sc0 sc1
	v_add_u32_e32 v235, 0x1000, v235
	global_store_dword v236, v45, s[46:47] sc0 sc1
	v_add_u32_e32 v236, 0x1000, v236
	v_fma_f32 v233, -v45, v1, v46
	v_fmac_f32_e32 v228, 0x3dcccccd, v233
	v_fma_f32 v46, s48, v228, v45
	global_store_dword v232, v46, s[18:19] sc0 sc1
	v_add_u32_e32 v232, 0x1000, v232
	global_store_dword v235, v228, s[44:45] sc0 sc1
	v_add_u32_e32 v235, 0x1000, v235
	global_store_dword v236, v46, s[46:47] sc0 sc1
	v_add_u32_e32 v236, 0x1000, v236
	v_fma_f32 v233, -v46, v1, v47
	v_fmac_f32_e32 v228, 0x3dcccccd, v233
	v_fma_f32 v47, s48, v228, v46
	global_store_dword v232, v47, s[18:19] sc0 sc1
	v_add_u32_e32 v232, 0x1000, v232
	global_store_dword v235, v228, s[44:45] sc0 sc1
	v_add_u32_e32 v235, 0x1000, v235
	global_store_dword v236, v47, s[46:47] sc0 sc1
	v_add_u32_e32 v236, 0x1000, v236
	v_fma_f32 v233, -v47, v1, v48
	v_fmac_f32_e32 v228, 0x3dcccccd, v233
	v_fma_f32 v48, s48, v228, v47
	global_store_dword v232, v48, s[18:19] sc0 sc1
	v_add_u32_e32 v232, 0x1000, v232
	global_store_dword v235, v228, s[44:45] sc0 sc1
	v_add_u32_e32 v235, 0x1000, v235
	global_store_dword v236, v48, s[46:47] sc0 sc1
	v_add_u32_e32 v236, 0x1000, v236
	v_fma_f32 v233, -v48, v1, v49
	v_fmac_f32_e32 v228, 0x3dcccccd, v233
	v_fma_f32 v49, s48, v228, v48
	global_store_dword v232, v49, s[18:19] sc0 sc1
	v_add_u32_e32 v232, 0x1000, v232
	global_store_dword v235, v228, s[44:45] sc0 sc1
	v_add_u32_e32 v235, 0x1000, v235
	global_store_dword v236, v49, s[46:47] sc0 sc1
	v_add_u32_e32 v236, 0x1000, v236
	v_fma_f32 v233, -v49, v1, v18
	v_fmac_f32_e32 v228, 0x3dcccccd, v233
	v_fma_f32 v18, s48, v228, v49
	global_store_dword v232, v18, s[18:19] sc0 sc1
	v_add_u32_e32 v232, 0x1000, v232
	global_store_dword v235, v228, s[44:45] sc0 sc1
	v_add_u32_e32 v235, 0x1000, v235
	global_store_dword v236, v18, s[46:47] sc0 sc1
	v_add_u32_e32 v236, 0x1000, v236
	v_fma_f32 v233, -v18, v1, v19
	v_fmac_f32_e32 v228, 0x3dcccccd, v233
	v_fma_f32 v19, s48, v228, v18
	global_store_dword v232, v19, s[18:19] sc0 sc1
	v_add_u32_e32 v232, 0x1000, v232
	global_store_dword v235, v228, s[44:45] sc0 sc1
	v_add_u32_e32 v235, 0x1000, v235
	global_store_dword v236, v19, s[46:47] sc0 sc1
	v_add_u32_e32 v236, 0x1000, v236
	v_fma_f32 v233, -v19, v1, v20
	v_fmac_f32_e32 v228, 0x3dcccccd, v233
	v_fma_f32 v20, s48, v228, v19
	global_store_dword v232, v20, s[18:19] sc0 sc1
	v_add_u32_e32 v232, 0x1000, v232
	global_store_dword v235, v228, s[44:45] sc0 sc1
	v_add_u32_e32 v235, 0x1000, v235
	global_store_dword v236, v20, s[46:47] sc0 sc1
	v_add_u32_e32 v236, 0x1000, v236
	v_fma_f32 v233, -v20, v1, v21
	v_fmac_f32_e32 v228, 0x3dcccccd, v233
	v_fma_f32 v21, s48, v228, v20
	global_store_dword v232, v21, s[18:19] sc0 sc1
	v_add_u32_e32 v232, 0x1000, v232
	global_store_dword v235, v228, s[44:45] sc0 sc1
	v_add_u32_e32 v235, 0x1000, v235
	global_store_dword v236, v21, s[46:47] sc0 sc1
	v_add_u32_e32 v236, 0x1000, v236
	v_fma_f32 v233, -v21, v1, v22
	v_fmac_f32_e32 v228, 0x3dcccccd, v233
	v_fma_f32 v22, s48, v228, v21
	global_store_dword v232, v22, s[18:19] sc0 sc1
	v_add_u32_e32 v232, 0x1000, v232
	global_store_dword v235, v228, s[44:45] sc0 sc1
	v_add_u32_e32 v235, 0x1000, v235
	global_store_dword v236, v22, s[46:47] sc0 sc1
	v_add_u32_e32 v236, 0x1000, v236
	v_fma_f32 v233, -v22, v1, v23
	v_fmac_f32_e32 v228, 0x3dcccccd, v233
	v_fma_f32 v23, s48, v228, v22
	global_store_dword v232, v23, s[18:19] sc0 sc1
	v_add_u32_e32 v232, 0x1000, v232
	global_store_dword v235, v228, s[44:45] sc0 sc1
	v_add_u32_e32 v235, 0x1000, v235
	global_store_dword v236, v23, s[46:47] sc0 sc1
	v_add_u32_e32 v236, 0x1000, v236
	v_fma_f32 v233, -v23, v1, v24
	v_fmac_f32_e32 v228, 0x3dcccccd, v233
	v_fma_f32 v24, s48, v228, v23
	global_store_dword v232, v24, s[18:19] sc0 sc1
	v_add_u32_e32 v232, 0x1000, v232
	global_store_dword v235, v228, s[44:45] sc0 sc1
	v_add_u32_e32 v235, 0x1000, v235
	global_store_dword v236, v24, s[46:47] sc0 sc1
	v_add_u32_e32 v236, 0x1000, v236
	v_fma_f32 v233, -v24, v1, v25
	v_fmac_f32_e32 v228, 0x3dcccccd, v233
	v_fma_f32 v25, s48, v228, v24
	global_store_dword v232, v25, s[18:19] sc0 sc1
	v_add_u32_e32 v232, 0x1000, v232
	global_store_dword v235, v228, s[44:45] sc0 sc1
	v_add_u32_e32 v235, 0x1000, v235
	global_store_dword v236, v25, s[46:47] sc0 sc1
	v_add_u32_e32 v236, 0x1000, v236
	v_fma_f32 v233, -v25, v1, v26
	v_fmac_f32_e32 v228, 0x3dcccccd, v233
	v_fma_f32 v26, s48, v228, v25
	global_store_dword v232, v26, s[18:19] sc0 sc1
	v_add_u32_e32 v232, 0x1000, v232
	global_store_dword v235, v228, s[44:45] sc0 sc1
	v_add_u32_e32 v235, 0x1000, v235
	global_store_dword v236, v26, s[46:47] sc0 sc1
	v_add_u32_e32 v236, 0x1000, v236
	v_fma_f32 v233, -v26, v1, v27
	v_fmac_f32_e32 v228, 0x3dcccccd, v233
	v_fma_f32 v27, s48, v228, v26
	global_store_dword v232, v27, s[18:19] sc0 sc1
	v_add_u32_e32 v232, 0x1000, v232
	global_store_dword v235, v228, s[44:45] sc0 sc1
	v_add_u32_e32 v235, 0x1000, v235
	global_store_dword v236, v27, s[46:47] sc0 sc1
	v_add_u32_e32 v236, 0x1000, v236
	v_fma_f32 v233, -v27, v1, v28
	v_fmac_f32_e32 v228, 0x3dcccccd, v233
	v_fma_f32 v28, s48, v228, v27
	global_store_dword v232, v28, s[18:19] sc0 sc1
	v_add_u32_e32 v232, 0x1000, v232
	global_store_dword v235, v228, s[44:45] sc0 sc1
	v_add_u32_e32 v235, 0x1000, v235
	global_store_dword v236, v28, s[46:47] sc0 sc1
	v_add_u32_e32 v236, 0x1000, v236
	v_fma_f32 v233, -v28, v1, v29
	v_fmac_f32_e32 v228, 0x3dcccccd, v233
	v_fma_f32 v29, s48, v228, v28
	global_store_dword v232, v29, s[18:19] sc0 sc1
	v_add_u32_e32 v232, 0x1000, v232
	global_store_dword v235, v228, s[44:45] sc0 sc1
	v_add_u32_e32 v235, 0x1000, v235
	global_store_dword v236, v29, s[46:47] sc0 sc1
	v_add_u32_e32 v236, 0x1000, v236
	v_fma_f32 v233, -v29, v1, v30
	v_fmac_f32_e32 v228, 0x3dcccccd, v233
	v_fma_f32 v30, s48, v228, v29
	global_store_dword v232, v30, s[18:19] sc0 sc1
	v_add_u32_e32 v232, 0x1000, v232
	global_store_dword v235, v228, s[44:45] sc0 sc1
	v_add_u32_e32 v235, 0x1000, v235
	global_store_dword v236, v30, s[46:47] sc0 sc1
	v_add_u32_e32 v236, 0x1000, v236
	v_fma_f32 v233, -v30, v1, v31
	v_fmac_f32_e32 v228, 0x3dcccccd, v233
	v_fma_f32 v31, s48, v228, v30
	global_store_dword v232, v31, s[18:19] sc0 sc1
	v_add_u32_e32 v232, 0x1000, v232
	global_store_dword v235, v228, s[44:45] sc0 sc1
	v_add_u32_e32 v235, 0x1000, v235
	global_store_dword v236, v31, s[46:47] sc0 sc1
	v_add_u32_e32 v236, 0x1000, v236
	v_fma_f32 v233, -v31, v1, v32
	v_fmac_f32_e32 v228, 0x3dcccccd, v233
	v_fma_f32 v32, s48, v228, v31
	global_store_dword v232, v32, s[18:19] sc0 sc1
	v_add_u32_e32 v232, 0x1000, v232
	global_store_dword v235, v228, s[44:45] sc0 sc1
	v_add_u32_e32 v235, 0x1000, v235
	global_store_dword v236, v32, s[46:47] sc0 sc1
	v_add_u32_e32 v236, 0x1000, v236
	v_fma_f32 v233, -v32, v1, v33
	v_fmac_f32_e32 v228, 0x3dcccccd, v233
	v_fma_f32 v33, s48, v228, v32
	global_store_dword v232, v33, s[18:19] sc0 sc1
	v_add_u32_e32 v232, 0x1000, v232
	global_store_dword v235, v228, s[44:45] sc0 sc1
	v_add_u32_e32 v235, 0x1000, v235
	global_store_dword v236, v33, s[46:47] sc0 sc1
	v_add_u32_e32 v236, 0x1000, v236
	v_fma_f32 v233, -v33, v1, v2
	v_fmac_f32_e32 v228, 0x3dcccccd, v233
	v_fma_f32 v2, s48, v228, v33
	global_store_dword v232, v2, s[18:19] sc0 sc1
	v_add_u32_e32 v232, 0x1000, v232
	global_store_dword v235, v228, s[44:45] sc0 sc1
	v_add_u32_e32 v235, 0x1000, v235
	global_store_dword v236, v2, s[46:47] sc0 sc1
	v_add_u32_e32 v236, 0x1000, v236
	v_fma_f32 v233, -v2, v1, v3
	v_fmac_f32_e32 v228, 0x3dcccccd, v233
	v_fma_f32 v3, s48, v228, v2
	global_store_dword v232, v3, s[18:19] sc0 sc1
	v_add_u32_e32 v232, 0x1000, v232
	global_store_dword v235, v228, s[44:45] sc0 sc1
	v_add_u32_e32 v235, 0x1000, v235
	global_store_dword v236, v3, s[46:47] sc0 sc1
	v_add_u32_e32 v236, 0x1000, v236
	v_fma_f32 v233, -v3, v1, v4
	v_fmac_f32_e32 v228, 0x3dcccccd, v233
	v_fma_f32 v4, s48, v228, v3
	global_store_dword v232, v4, s[18:19] sc0 sc1
	v_add_u32_e32 v232, 0x1000, v232
	global_store_dword v235, v228, s[44:45] sc0 sc1
	v_add_u32_e32 v235, 0x1000, v235
	global_store_dword v236, v4, s[46:47] sc0 sc1
	v_add_u32_e32 v236, 0x1000, v236
	v_fma_f32 v233, -v4, v1, v5
	v_fmac_f32_e32 v228, 0x3dcccccd, v233
	v_fma_f32 v5, s48, v228, v4
	global_store_dword v232, v5, s[18:19] sc0 sc1
	v_add_u32_e32 v232, 0x1000, v232
	global_store_dword v235, v228, s[44:45] sc0 sc1
	v_add_u32_e32 v235, 0x1000, v235
	global_store_dword v236, v5, s[46:47] sc0 sc1
	v_add_u32_e32 v236, 0x1000, v236
	v_fma_f32 v233, -v5, v1, v6
	v_fmac_f32_e32 v228, 0x3dcccccd, v233
	v_fma_f32 v6, s48, v228, v5
	global_store_dword v232, v6, s[18:19] sc0 sc1
	v_add_u32_e32 v232, 0x1000, v232
	global_store_dword v235, v228, s[44:45] sc0 sc1
	v_add_u32_e32 v235, 0x1000, v235
	global_store_dword v236, v6, s[46:47] sc0 sc1
	v_add_u32_e32 v236, 0x1000, v236
	v_fma_f32 v233, -v6, v1, v7
	v_fmac_f32_e32 v228, 0x3dcccccd, v233
	v_fma_f32 v7, s48, v228, v6
	global_store_dword v232, v7, s[18:19] sc0 sc1
	v_add_u32_e32 v232, 0x1000, v232
	global_store_dword v235, v228, s[44:45] sc0 sc1
	v_add_u32_e32 v235, 0x1000, v235
	global_store_dword v236, v7, s[46:47] sc0 sc1
	v_add_u32_e32 v236, 0x1000, v236
	v_fma_f32 v233, -v7, v1, v8
	v_fmac_f32_e32 v228, 0x3dcccccd, v233
	v_fma_f32 v8, s48, v228, v7
	global_store_dword v232, v8, s[18:19] sc0 sc1
	v_add_u32_e32 v232, 0x1000, v232
	global_store_dword v235, v228, s[44:45] sc0 sc1
	v_add_u32_e32 v235, 0x1000, v235
	global_store_dword v236, v8, s[46:47] sc0 sc1
	v_add_u32_e32 v236, 0x1000, v236
	v_fma_f32 v233, -v8, v1, v9
	v_fmac_f32_e32 v228, 0x3dcccccd, v233
	v_fma_f32 v9, s48, v228, v8
	global_store_dword v232, v9, s[18:19] sc0 sc1
	v_add_u32_e32 v232, 0x1000, v232
	global_store_dword v235, v228, s[44:45] sc0 sc1
	v_add_u32_e32 v235, 0x1000, v235
	global_store_dword v236, v9, s[46:47] sc0 sc1
	v_add_u32_e32 v236, 0x1000, v236
	v_fma_f32 v233, -v9, v1, v10
	v_fmac_f32_e32 v228, 0x3dcccccd, v233
	v_fma_f32 v10, s48, v228, v9
	global_store_dword v232, v10, s[18:19] sc0 sc1
	v_add_u32_e32 v232, 0x1000, v232
	global_store_dword v235, v228, s[44:45] sc0 sc1
	v_add_u32_e32 v235, 0x1000, v235
	global_store_dword v236, v10, s[46:47] sc0 sc1
	v_add_u32_e32 v236, 0x1000, v236
	v_fma_f32 v233, -v10, v1, v11
	v_fmac_f32_e32 v228, 0x3dcccccd, v233
	v_fma_f32 v11, s48, v228, v10
	global_store_dword v232, v11, s[18:19] sc0 sc1
	v_add_u32_e32 v232, 0x1000, v232
	global_store_dword v235, v228, s[44:45] sc0 sc1
	v_add_u32_e32 v235, 0x1000, v235
	global_store_dword v236, v11, s[46:47] sc0 sc1
	v_add_u32_e32 v236, 0x1000, v236
	v_fma_f32 v233, -v11, v1, v12
	v_fmac_f32_e32 v228, 0x3dcccccd, v233
	v_fma_f32 v12, s48, v228, v11
	global_store_dword v232, v12, s[18:19] sc0 sc1
	v_add_u32_e32 v232, 0x1000, v232
	global_store_dword v235, v228, s[44:45] sc0 sc1
	v_add_u32_e32 v235, 0x1000, v235
	global_store_dword v236, v12, s[46:47] sc0 sc1
	v_add_u32_e32 v236, 0x1000, v236
	v_fma_f32 v233, -v12, v1, v13
	v_fmac_f32_e32 v228, 0x3dcccccd, v233
	v_fma_f32 v13, s48, v228, v12
	global_store_dword v232, v13, s[18:19] sc0 sc1
	v_add_u32_e32 v232, 0x1000, v232
	global_store_dword v235, v228, s[44:45] sc0 sc1
	v_add_u32_e32 v235, 0x1000, v235
	global_store_dword v236, v13, s[46:47] sc0 sc1
	v_add_u32_e32 v236, 0x1000, v236
	v_fma_f32 v233, -v13, v1, v14
	v_fmac_f32_e32 v228, 0x3dcccccd, v233
	v_fma_f32 v14, s48, v228, v13
	global_store_dword v232, v14, s[18:19] sc0 sc1
	v_add_u32_e32 v232, 0x1000, v232
	global_store_dword v235, v228, s[44:45] sc0 sc1
	v_add_u32_e32 v235, 0x1000, v235
	global_store_dword v236, v14, s[46:47] sc0 sc1
	v_add_u32_e32 v236, 0x1000, v236
	v_fma_f32 v233, -v14, v1, v15
	v_fmac_f32_e32 v228, 0x3dcccccd, v233
	v_fma_f32 v15, s48, v228, v14
	global_store_dword v232, v15, s[18:19] sc0 sc1
	v_add_u32_e32 v232, 0x1000, v232
	global_store_dword v235, v228, s[44:45] sc0 sc1
	v_add_u32_e32 v235, 0x1000, v235
	global_store_dword v236, v15, s[46:47] sc0 sc1
	v_add_u32_e32 v236, 0x1000, v236
	v_fma_f32 v233, -v15, v1, v16
	v_fmac_f32_e32 v228, 0x3dcccccd, v233
	v_fma_f32 v16, s48, v228, v15
	global_store_dword v232, v16, s[18:19] sc0 sc1
	v_add_u32_e32 v232, 0x1000, v232
	global_store_dword v235, v228, s[44:45] sc0 sc1
	v_add_u32_e32 v235, 0x1000, v235
	global_store_dword v236, v16, s[46:47] sc0 sc1
	v_add_u32_e32 v236, 0x1000, v236
	v_fma_f32 v233, -v16, v1, v17
	v_fmac_f32_e32 v228, 0x3dcccccd, v233
	v_fma_f32 v17, s48, v228, v16
	global_store_dword v232, v17, s[18:19] sc0 sc1
	v_add_u32_e32 v232, 0x1000, v232
	global_store_dword v235, v228, s[44:45] sc0 sc1
	v_add_u32_e32 v235, 0x1000, v235
	global_store_dword v236, v17, s[46:47] sc0 sc1
	v_add_u32_e32 v236, 0x1000, v236
	s_endpgm
